# q3 + second half K fragments prefetched 2-4 MFMAs ahead into own registers
# speedup vs baseline: 1.0029x; 1.0029x over previous
; #define PK4(P, BASE, OUT) do { u32x4 w = {cvt_pk_bf16(P[BASE + 0], P[BASE + 1]), cvt_pk_bf16(P[BASE + 2], P[BASE + 3]), cvt_pk_bf16(P[BASE + 4], P[BASE + 5]), cvt_pk_bf16(P[BASE + 6], P[BASE + 7])}; \
;     OUT = *reinterpret_cast<bf16x8*>(&w); } while (0)
; DEVI void finishSM(f32x16& p0, f32x16& p1, float alpha, float& l_reg, bf16x8& pa0, bf16x8& pa1, bf16x8& pa2, bf16x8& pa3) {
; #pragma unroll
;     for (int r = 0; r < 16; ++r) p1[r] = __builtin_amdgcn_exp2f(p1[r]);
;     f32x2 s2 = (f32x2){p0[0], p0[1]} + (f32x2){p1[0], p1[1]};
; #pragma unroll
;     for (int r = 2; r < 16; r += 2) s2 += (f32x2){p0[r], p0[r + 1]} + (f32x2){p1[r], p1[r + 1]};
;     float ps = s2[0] + s2[1];
;     { auto rr = __builtin_amdgcn_permlane32_swap(__float_as_uint(ps), __float_as_uint(ps), false, false);
;       ps = __uint_as_float(rr[0]) + __uint_as_float(rr[1]); }
;     l_reg = l_reg * alpha + ps;
;     ...
;     PK4(p0, 0, pa0); PK4(p0, 8, pa1); PK4(p1, 0, pa2); PK4(p1, 8, pa3);
;     ...
; }
; DEVI void qkt(f32x16& p0, f32x16& p1, const char* Kb, const bf16x8 (&qr)[6], int r32, int hi, const f32x16& cinit) {
; #pragma unroll
;     for (int d0 = 0; d0 < 6; ++d0) { const int cb = (d0 * 16 + hi * 8) * 2;
;         const bf16x8 k0 = *(const bf16x8*)(Kb + KSWZ(r32, cb)), k1 = *(const bf16x8*)(Kb + KSWZ(32 + r32, cb));
;         p0 = __builtin_amdgcn_mfma_f32_32x32x16_bf16(k0, qr[d0], d0 == 0 ? cinit : p0, 0, 0, 0);
;         p1 = __builtin_amdgcn_mfma_f32_32x32x16_bf16(k1, qr[d0], d0 == 0 ? cinit : p1, 0, 0, 0); }
; }
.LBB0_702:
	s_mul_i32 s98, s2, 0x6000
	s_add_i32 s98, s96, s98
	s_lshl_b32 s99, s2, 14
	s_add_i32 s99, s97, s99
	s_mul_i32 s6, s61, 0x6000
	s_add_i32 s6, s6, 0
	v_add_u32_e32 v86, s6, v129
	v_lshl_add_u64 v[250:251], v[118:119], 0, s[12:13]
	s_mov_b32 m0, s98
	s_barrier
	ds_read_b128 v[82:85], v86
	ds_read_b128 v[210:213], v86 offset:6144
	v_add_u32_e32 v126, s6, v184
	ds_read_b128 v[154:157], v126
	ds_read_b128 v[214:217], v126 offset:6144
	global_load_lds_dwordx4 v[250:251], off
	v_exp_f32_e32 v66, v66
	s_waitcnt lgkmcnt(3)
	v_mfma_f32_32x32x16_bf16 v[98:113], v[82:85], v[150:153], v[34:49]
	v_add_u32_e32 v126, s6, v185
	ds_read_b128 v[158:161], v126
	ds_read_b128 v[162:165], v126 offset:6144
	v_lshl_add_u64 v[250:251], v[120:121], 0, s[12:13]
	s_add_i32 m0, s98, 0x2000
	v_exp_f32_e32 v67, v67
	v_exp_f32_e32 v68, v68
	global_load_lds_dwordx4 v[250:251], off
	v_exp_f32_e32 v69, v69
	v_exp_f32_e32 v70, v70
	v_exp_f32_e32 v71, v71
	v_exp_f32_e32 v72, v72
	s_waitcnt lgkmcnt(4)
	v_mfma_f32_32x32x16_bf16 v[82:97], v[210:213], v[150:153], v[34:49]
	v_add_u32_e32 v126, s6, v204
	ds_read_b128 v[166:169], v126
	ds_read_b128 v[218:221], v126 offset:6144
	v_lshl_add_u64 v[250:251], v[122:123], 0, s[12:13]
	s_add_i32 m0, s98, 0x4000
	v_exp_f32_e32 v73, v73
	v_exp_f32_e32 v74, v74
	global_load_lds_dwordx4 v[250:251], off
	v_exp_f32_e32 v75, v75
	v_exp_f32_e32 v76, v76
	v_exp_f32_e32 v77, v77
	s_waitcnt lgkmcnt(5)
	v_mfma_f32_32x32x16_bf16 v[98:113], v[154:157], v[138:141], v[98:113]
	v_add_u32_e32 v126, s6, v205
	ds_read_b128 v[234:237], v126
	ds_read_b128 v[222:225], v126 offset:6144
	s_mov_b32 m0, s99
	v_exp_f32_e32 v78, v78
	v_exp_f32_e32 v79, v79
	v_lshl_add_u64 v[250:251], v[116:117], 0, s[40:41]
	global_load_lds_dwordx4 v[116:117], off
	s_add_i32 m0, s99, 0x2000
	v_exp_f32_e32 v80, v80
	v_exp_f32_e32 v81, v81
	v_add_u32_e32 v174, 0x2000, v202
	global_load_lds_dwordx4 v[250:251], off
	s_waitcnt lgkmcnt(6)
	v_mfma_f32_32x32x16_bf16 v[82:97], v[214:217], v[138:141], v[82:97]
	v_add_u32_e32 v126, s6, v206
	ds_read_b128 v[226:229], v126
	ds_read_b128 v[230:233], v126 offset:6144
	s_waitcnt lgkmcnt(7)
	v_mfma_f32_32x32x16_bf16 v[98:113], v[158:161], v[134:137], v[98:113]
	s_waitcnt lgkmcnt(6)
	v_mfma_f32_32x32x16_bf16 v[82:97], v[162:165], v[134:137], v[82:97]
	v_add_f32_e32 v126, v50, v66
	v_add_f32_e32 v127, v51, v67
	v_cvt_pk_bf16_f32 v50, v50, v51
	v_cvt_pk_bf16_f32 v51, v52, v53
	s_waitcnt lgkmcnt(5)
	v_mfma_f32_32x32x16_bf16 v[98:113], v[166:169], v[130:133], v[98:113]
	v_add_f32_e64 v210, v52, v68
	v_add_f32_e64 v211, v53, v69
	v_cvt_pk_bf16_f32 v52, v54, v55
	v_cvt_pk_bf16_f32 v53, v56, v57
	v_add_f32_e64 v126, v210, v126
	v_add_f32_e64 v127, v211, v127
	v_add_f32_e64 v210, v54, v70
	v_add_f32_e64 v211, v55, v71
	v_cvt_pk_bf16_f32 v54, v58, v59
	s_waitcnt lgkmcnt(4)
	v_mfma_f32_32x32x16_bf16 v[82:97], v[218:221], v[130:133], v[82:97]
	v_add_f32_e64 v126, v210, v126
	v_add_f32_e64 v127, v211, v127
	v_add_f32_e64 v210, v56, v72
	v_add_f32_e64 v211, v57, v73
	v_cvt_pk_bf16_f32 v55, v60, v61
	v_cvt_pk_bf16_f32 v56, v62, v63
	v_cvt_pk_bf16_f32 v57, v64, v65
	v_add_f32_e64 v126, v210, v126
	v_add_f32_e64 v127, v211, v127
	v_add_f32_e32 v210, v58, v74
	v_add_f32_e32 v211, v59, v75
	v_cvt_pk_bf16_f32 v58, v66, v67
	v_cvt_pk_bf16_f32 v59, v68, v69
	s_waitcnt lgkmcnt(3)
	v_mfma_f32_32x32x16_bf16 v[98:113], v[234:237], v[146:149], v[98:113]
	v_add_f32_e64 v126, v210, v126
	v_add_f32_e64 v127, v211, v127
	v_add_f32_e64 v210, v60, v76
	v_add_f32_e64 v211, v61, v77
	v_cvt_pk_bf16_f32 v60, v70, v71
	v_cvt_pk_bf16_f32 v61, v72, v73
	v_add_f32_e64 v126, v210, v126
	v_add_f32_e64 v127, v211, v127
	v_add_f32_e32 v210, v62, v78
	v_add_f32_e32 v211, v63, v79
	v_cvt_pk_bf16_f32 v62, v74, v75
	v_cvt_pk_bf16_f32 v63, v76, v77
	s_waitcnt lgkmcnt(2)
; DEVI void pv_both(f32x16& o0, f32x16& o1, int vb, bf16x8 pa0, bf16x8 pa1, bf16x8 pa2, bf16x8 pa3) {
;     const s16x4 a0 = tr_read<v_rd_off(0, 0, 0)>(vb), b0 = tr_read<v_rd_off(0, 0, 1)>(vb), a1 = tr_read<v_rd_off(0, 1, 0)>(vb), b1 = tr_read<v_rd_off(0, 1, 1)>(vb);
;     const s16x4 a2 = tr_read<v_rd_off(0, 2, 0)>(vb), b2 = tr_read<v_rd_off(0, 2, 1)>(vb), a3 = tr_read<v_rd_off(0, 3, 0)>(vb), b3 = tr_read<v_rd_off(0, 3, 1)>(vb);
;     const s16x4 c0 = tr_read<v_rd_off(1, 0, 0)>(vb), d0 = tr_read<v_rd_off(1, 0, 1)>(vb), c1 = tr_read<v_rd_off(1, 1, 0)>(vb), d1 = tr_read<v_rd_off(1, 1, 1)>(vb);
;     const s16x4 c2 = tr_read<v_rd_off(1, 2, 0)>(vb), d2 = tr_read<v_rd_off(1, 2, 1)>(vb), c3 = tr_read<v_rd_off(1, 3, 0)>(vb), d3 = tr_read<v_rd_off(1, 3, 1)>(vb);
;     asm volatile("s_waitcnt lgkmcnt(8)" ::: "memory"); SBAR();
;     ...
;     o0 = __builtin_amdgcn_mfma_f32_32x32x16_bf16(pa0, PK(a0, b0), o0, 0, 0, 0);
;     o0 = __builtin_amdgcn_mfma_f32_32x32x16_bf16(pa1, PK(a1, b1), o0, 0, 0, 0);
;     o0 = __builtin_amdgcn_mfma_f32_32x32x16_bf16(pa2, PK(a2, b2), o0, 0, 0, 0);
;     o0 = __builtin_amdgcn_mfma_f32_32x32x16_bf16(pa3, PK(a3, b3), o0, 0, 0, 0);
;     asm volatile("s_waitcnt lgkmcnt(0)" ::: "memory"); SBAR();
;     o1 = __builtin_amdgcn_mfma_f32_32x32x16_bf16(pa0, PK(c0, d0), o1, 0, 0, 0);
;     o1 = __builtin_amdgcn_mfma_f32_32x32x16_bf16(pa1, PK(c1, d1), o1, 0, 0, 0);
;     o1 = __builtin_amdgcn_mfma_f32_32x32x16_bf16(pa2, PK(c2, d2), o1, 0, 0, 0);
;     o1 = __builtin_amdgcn_mfma_f32_32x32x16_bf16(pa3, PK(c3, d3), o1, 0, 0, 0);
;     ...
; }
; template <bool FIRST> DEVI bool partialSM(f32x16& p0, f32x16& p1, float& m_reg, float& alpha) {
;     float pmax = p0[0];
; #pragma unroll
;     for (int r = 1; r < 16; ++r) pmax = fmaxf(pmax, p0[r]);
; #pragma unroll
;     for (int r = 0; r < 16; ++r) pmax = fmaxf(pmax, p1[r]);
;     { auto rr = __builtin_amdgcn_permlane32_swap(__float_as_uint(pmax), __float_as_uint(pmax), false, false);
;       pmax = fmaxf(__uint_as_float(rr[0]), __uint_as_float(rr[1])); }
;     if (FIRST) { m_reg = pmax; alpha = 1.f;
; #pragma unroll
;         for (int r = 0; r < 16; ++r) { p0[r] = __builtin_amdgcn_exp2f(p0[r] - pmax); p1[r] = p1[r] - pmax; }
;         return false;
;     } else if (__builtin_expect(__all(pmax <= ATT_THR), 1)) { alpha = 1.f;
; #pragma unroll
;         for (int r = 0; r < 16; ++r) p0[r] = __builtin_amdgcn_exp2f(p0[r]);
	v_mfma_f32_32x32x16_bf16 v[82:97], v[222:225], v[146:149], v[82:97]
	v_add_f32_e64 v126, v210, v126
	v_add_f32_e64 v127, v211, v127
	v_add_f32_e64 v210, v64, v80
	v_add_f32_e64 v211, v65, v81
	v_cvt_pk_bf16_f32 v64, v78, v79
	v_cvt_pk_bf16_f32 v65, v80, v81
	ds_read_b64_tr_b16 v[66:67], v174 offset:0
	ds_read_b64_tr_b16 v[68:69], v174 offset:0x400
	ds_read_b64_tr_b16 v[70:71], v174 offset:0x800
	ds_read_b64_tr_b16 v[72:73], v174 offset:0xc00
	ds_read_b64_tr_b16 v[74:75], v174 offset:0x1000
	ds_read_b64_tr_b16 v[76:77], v174 offset:0x1400
	ds_read_b64_tr_b16 v[78:79], v174 offset:0x1800
	ds_read_b64_tr_b16 v[80:81], v174 offset:0x1c00
	v_add_f32_e64 v126, v210, v126
	v_add_f32_e64 v127, v211, v127
	ds_read_b64_tr_b16 v[210:211], v174 offset:0x200
	ds_read_b64_tr_b16 v[212:213], v174 offset:0x600
	ds_read_b64_tr_b16 v[214:215], v174 offset:0xa00
	s_waitcnt lgkmcnt(12)
	v_mfma_f32_32x32x16_bf16 v[98:113], v[226:229], v[142:145], v[98:113]
	ds_read_b64_tr_b16 v[216:217], v174 offset:0xe00
	ds_read_b64_tr_b16 v[218:219], v174 offset:0x1200
	ds_read_b64_tr_b16 v[220:221], v174 offset:0x1600
	ds_read_b64_tr_b16 v[222:223], v174 offset:0x1a00
	ds_read_b64_tr_b16 v[224:225], v174 offset:0x1e00
	v_add_f32_e32 v126, v126, v127
	s_waitcnt lgkmcnt(15)
	v_mfma_f32_32x32x16_bf16 v[82:97], v[230:233], v[142:145], v[82:97]
	v_mov_b32_e32 v127, v126
	s_nop 1
	v_permlane32_swap_b32_e32 v126, v127
	s_waitcnt lgkmcnt(14)
	v_mfma_f32_32x32x16_bf16 v[18:33], v[50:53], v[66:69], v[18:33]
	s_waitcnt lgkmcnt(6)
	v_mfma_f32_32x32x16_bf16 v[2:17], v[50:53], v[210:213], v[2:17]
	s_nop 4
	v_max_f32_e32 v249, v99, v99
	v_max_f32_e32 v250, v98, v98
	v_max_f32_e32 v249, v250, v249
	v_max3_f32 v249, v249, v100, v101
	v_max3_f32 v249, v249, v102, v103
	v_max3_f32 v251, v249, v104, v105
	v_max3_f32 v251, v251, v106, v107
	v_exp_f32_e32 v50, v98
	v_exp_f32_e32 v51, v99
	v_exp_f32_e32 v52, v100
	v_exp_f32_e32 v53, v101
	v_mov_b64_e32 v[66:67], v[82:83]
	v_mov_b64_e32 v[68:69], v[84:85]
	v_mfma_f32_32x32x16_bf16 v[18:33], v[54:57], v[70:73], v[18:33]
	s_waitcnt lgkmcnt(4)
	v_mfma_f32_32x32x16_bf16 v[2:17], v[54:57], v[214:217], v[2:17]
	v_max3_f32 v251, v251, v108, v109
	v_max3_f32 v251, v251, v110, v111
	v_max3_f32 v251, v251, v112, v113
	v_max3_f32 v251, v251, v82, v83
	v_max3_f32 v251, v251, v84, v85
	v_max3_f32 v251, v251, v86, v87
	v_max3_f32 v251, v251, v88, v89
	v_exp_f32_e32 v54, v102
	v_exp_f32_e32 v55, v103
	v_exp_f32_e32 v56, v104
	v_exp_f32_e32 v57, v105
	v_mov_b64_e32 v[70:71], v[86:87]
	v_mov_b64_e32 v[72:73], v[88:89]
	v_mfma_f32_32x32x16_bf16 v[18:33], v[58:61], v[74:77], v[18:33]
	s_waitcnt lgkmcnt(2)
	v_mfma_f32_32x32x16_bf16 v[2:17], v[58:61], v[218:221], v[2:17]
	v_max3_f32 v251, v251, v90, v91
	v_max3_f32 v251, v251, v92, v93
	v_max3_f32 v251, v251, v94, v95
	v_max3_f32 v251, v251, v96, v97
	v_mov_b32_e32 v252, v251
	s_nop 1
	v_permlane32_swap_b32_e32 v251, v252
	v_exp_f32_e32 v58, v106
	v_exp_f32_e32 v59, v107
	v_exp_f32_e32 v60, v108
	v_exp_f32_e32 v61, v109
	v_mov_b64_e32 v[74:75], v[90:91]
	v_mov_b64_e32 v[76:77], v[92:93]
	v_mfma_f32_32x32x16_bf16 v[18:33], v[62:65], v[78:81], v[18:33]
	s_waitcnt lgkmcnt(0)
	v_mfma_f32_32x32x16_bf16 v[2:17], v[62:65], v[222:225], v[2:17]
	v_exp_f32_e32 v62, v110
	v_exp_f32_e32 v63, v111
	v_exp_f32_e32 v64, v112
	v_exp_f32_e32 v65, v113
	v_mov_b64_e32 v[78:79], v[94:95]
	v_mov_b64_e32 v[80:81], v[96:97]
	v_max_f32_e32 v252, v252, v252
	v_max_f32_e32 v251, v251, v251
	v_max_f32_e32 v174, v251, v252
	v_cmp_ge_f32_e32 vcc, s79, v174
	s_cmp_lg_u64 vcc, exec
	s_cselect_b64 s[6:7], -1, 0
	s_cbranch_scc1 .LBB0_711
	v_mov_b32_e32 v202, 1.0
	v_mov_b32_e32 v203, v209
	s_branch .LBB0_716

; #define PK4(P, BASE, OUT) do { u32x4 w = {cvt_pk_bf16(P[BASE + 0], P[BASE + 1]), cvt_pk_bf16(P[BASE + 2], P[BASE + 3]), cvt_pk_bf16(P[BASE + 4], P[BASE + 5]), cvt_pk_bf16(P[BASE + 6], P[BASE + 7])}; \
;     OUT = *reinterpret_cast<bf16x8*>(&w); } while (0)
; DEVI void finishSM(f32x16& p0, f32x16& p1, float alpha, float& l_reg, bf16x8& pa0, bf16x8& pa1, bf16x8& pa2, bf16x8& pa3) {
; #pragma unroll
;     for (int r = 0; r < 16; ++r) p1[r] = __builtin_amdgcn_exp2f(p1[r]);
;     f32x2 s2 = (f32x2){p0[0], p0[1]} + (f32x2){p1[0], p1[1]};
; #pragma unroll
;     for (int r = 2; r < 16; r += 2) s2 += (f32x2){p0[r], p0[r + 1]} + (f32x2){p1[r], p1[r + 1]};
;     float ps = s2[0] + s2[1];
;     { auto rr = __builtin_amdgcn_permlane32_swap(__float_as_uint(ps), __float_as_uint(ps), false, false);
;       ps = __uint_as_float(rr[0]) + __uint_as_float(rr[1]); }
;     l_reg = l_reg * alpha + ps;
;     ...
;     PK4(p0, 0, pa0); PK4(p0, 8, pa1); PK4(p1, 0, pa2); PK4(p1, 8, pa3);
;     ...
; }
; DEVI void qkt(f32x16& p0, f32x16& p1, const char* Kb, const bf16x8 (&qr)[6], int r32, int hi, const f32x16& cinit) {
; #pragma unroll
;     for (int d0 = 0; d0 < 6; ++d0) { const int cb = (d0 * 16 + hi * 8) * 2;
;         const bf16x8 k0 = *(const bf16x8*)(Kb + KSWZ(r32, cb)), k1 = *(const bf16x8*)(Kb + KSWZ(32 + r32, cb));
;         p0 = __builtin_amdgcn_mfma_f32_32x32x16_bf16(k0, qr[d0], d0 == 0 ? cinit : p0, 0, 0, 0);
;         p1 = __builtin_amdgcn_mfma_f32_32x32x16_bf16(k1, qr[d0], d0 == 0 ? cinit : p1, 0, 0, 0); }
; }
.LBB0_2266:
	s_mul_i32 s98, s61, 0x6000
	s_add_i32 s98, s96, s98
	s_lshl_b32 s99, s61, 14
	s_add_i32 s99, s97, s99
	s_mul_i32 s6, s2, 0x6000
	s_add_i32 s6, s6, 0
	v_add_u32_e32 v86, s6, v129
	v_lshl_add_u64 v[250:251], v[118:119], 0, s[12:13]
	s_mov_b32 m0, s98
	s_barrier
	ds_read_b128 v[82:85], v86
	ds_read_b128 v[212:215], v86 offset:6144
	v_add_u32_e32 v126, s6, v184
	ds_read_b128 v[154:157], v126
	ds_read_b128 v[216:219], v126 offset:6144
	global_load_lds_dwordx4 v[250:251], off
	v_exp_f32_e32 v66, v66
	s_waitcnt lgkmcnt(3)
	v_mfma_f32_32x32x16_bf16 v[98:113], v[82:85], v[150:153], v[34:49]
	v_add_u32_e32 v126, s6, v185
	ds_read_b128 v[158:161], v126
	ds_read_b128 v[162:165], v126 offset:6144
	v_lshl_add_u64 v[250:251], v[120:121], 0, s[12:13]
	s_add_i32 m0, s98, 0x2000
	v_exp_f32_e32 v67, v67
	v_exp_f32_e32 v68, v68
	global_load_lds_dwordx4 v[250:251], off
	v_exp_f32_e32 v69, v69
	v_exp_f32_e32 v70, v70
	v_exp_f32_e32 v71, v71
	v_exp_f32_e32 v72, v72
	s_waitcnt lgkmcnt(4)
	v_mfma_f32_32x32x16_bf16 v[82:97], v[212:215], v[150:153], v[34:49]
	v_add_u32_e32 v126, s6, v205
	ds_read_b128 v[166:169], v126
	ds_read_b128 v[220:223], v126 offset:6144
	v_lshl_add_u64 v[250:251], v[122:123], 0, s[12:13]
	s_add_i32 m0, s98, 0x4000
	v_exp_f32_e32 v73, v73
	v_exp_f32_e32 v74, v74
	global_load_lds_dwordx4 v[250:251], off
	v_exp_f32_e32 v75, v75
	v_exp_f32_e32 v76, v76
	v_exp_f32_e32 v77, v77
	s_waitcnt lgkmcnt(5)
	v_mfma_f32_32x32x16_bf16 v[98:113], v[154:157], v[138:141], v[98:113]
	v_add_u32_e32 v126, s6, v206
	ds_read_b128 v[234:237], v126
	ds_read_b128 v[224:227], v126 offset:6144
	s_mov_b32 m0, s99
	v_exp_f32_e32 v78, v78
	v_exp_f32_e32 v79, v79
	v_lshl_add_u64 v[250:251], v[116:117], 0, s[40:41]
	global_load_lds_dwordx4 v[116:117], off
	s_add_i32 m0, s99, 0x2000
	v_exp_f32_e32 v80, v80
	v_exp_f32_e32 v81, v81
	v_add_u32_e32 v174, 0x2000, v203
	global_load_lds_dwordx4 v[250:251], off
	s_waitcnt lgkmcnt(6)
	v_mfma_f32_32x32x16_bf16 v[82:97], v[216:219], v[138:141], v[82:97]
	v_add_u32_e32 v126, s6, v207
	ds_read_b128 v[228:231], v126
	ds_read_b128 v[232:235], v126 offset:6144
	s_waitcnt lgkmcnt(7)
	v_mfma_f32_32x32x16_bf16 v[98:113], v[158:161], v[134:137], v[98:113]
	s_waitcnt lgkmcnt(6)
	v_mfma_f32_32x32x16_bf16 v[82:97], v[162:165], v[134:137], v[82:97]
	v_add_f32_e32 v126, v50, v66
	v_add_f32_e32 v127, v51, v67
	v_cvt_pk_bf16_f32 v50, v50, v51
	v_cvt_pk_bf16_f32 v51, v52, v53
	s_waitcnt lgkmcnt(5)
	v_mfma_f32_32x32x16_bf16 v[98:113], v[166:169], v[130:133], v[98:113]
	v_add_f32_e64 v212, v52, v68
	v_add_f32_e64 v213, v53, v69
	v_cvt_pk_bf16_f32 v52, v54, v55
	v_cvt_pk_bf16_f32 v53, v56, v57
	v_add_f32_e64 v126, v212, v126
	v_add_f32_e64 v127, v213, v127
	v_add_f32_e64 v212, v54, v70
	v_add_f32_e64 v213, v55, v71
	v_cvt_pk_bf16_f32 v54, v58, v59
	s_waitcnt lgkmcnt(4)
	v_mfma_f32_32x32x16_bf16 v[82:97], v[220:223], v[130:133], v[82:97]
	v_add_f32_e64 v126, v212, v126
	v_add_f32_e64 v127, v213, v127
	v_add_f32_e64 v212, v56, v72
	v_add_f32_e64 v213, v57, v73
	v_cvt_pk_bf16_f32 v55, v60, v61
	v_cvt_pk_bf16_f32 v56, v62, v63
	v_cvt_pk_bf16_f32 v57, v64, v65
	v_add_f32_e64 v126, v212, v126
	v_add_f32_e64 v127, v213, v127
	v_add_f32_e32 v212, v58, v74
	v_add_f32_e32 v213, v59, v75
	v_cvt_pk_bf16_f32 v58, v66, v67
	v_cvt_pk_bf16_f32 v59, v68, v69
	s_waitcnt lgkmcnt(0)
; DEVI void pv_both(f32x16& o0, f32x16& o1, int vb, bf16x8 pa0, bf16x8 pa1, bf16x8 pa2, bf16x8 pa3) {
;     const s16x4 a0 = tr_read<v_rd_off(0, 0, 0)>(vb), b0 = tr_read<v_rd_off(0, 0, 1)>(vb), a1 = tr_read<v_rd_off(0, 1, 0)>(vb), b1 = tr_read<v_rd_off(0, 1, 1)>(vb);
;     const s16x4 a2 = tr_read<v_rd_off(0, 2, 0)>(vb), b2 = tr_read<v_rd_off(0, 2, 1)>(vb), a3 = tr_read<v_rd_off(0, 3, 0)>(vb), b3 = tr_read<v_rd_off(0, 3, 1)>(vb);
;     const s16x4 c0 = tr_read<v_rd_off(1, 0, 0)>(vb), d0 = tr_read<v_rd_off(1, 0, 1)>(vb), c1 = tr_read<v_rd_off(1, 1, 0)>(vb), d1 = tr_read<v_rd_off(1, 1, 1)>(vb);
;     const s16x4 c2 = tr_read<v_rd_off(1, 2, 0)>(vb), d2 = tr_read<v_rd_off(1, 2, 1)>(vb), c3 = tr_read<v_rd_off(1, 3, 0)>(vb), d3 = tr_read<v_rd_off(1, 3, 1)>(vb);
;     asm volatile("s_waitcnt lgkmcnt(8)" ::: "memory"); SBAR();
;     ...
;     o0 = __builtin_amdgcn_mfma_f32_32x32x16_bf16(pa0, PK(a0, b0), o0, 0, 0, 0);
;     o0 = __builtin_amdgcn_mfma_f32_32x32x16_bf16(pa1, PK(a1, b1), o0, 0, 0, 0);
;     o0 = __builtin_amdgcn_mfma_f32_32x32x16_bf16(pa2, PK(a2, b2), o0, 0, 0, 0);
;     o0 = __builtin_amdgcn_mfma_f32_32x32x16_bf16(pa3, PK(a3, b3), o0, 0, 0, 0);
;     asm volatile("s_waitcnt lgkmcnt(0)" ::: "memory"); SBAR();
;     o1 = __builtin_amdgcn_mfma_f32_32x32x16_bf16(pa0, PK(c0, d0), o1, 0, 0, 0);
;     o1 = __builtin_amdgcn_mfma_f32_32x32x16_bf16(pa1, PK(c1, d1), o1, 0, 0, 0);
;     o1 = __builtin_amdgcn_mfma_f32_32x32x16_bf16(pa2, PK(c2, d2), o1, 0, 0, 0);
;     o1 = __builtin_amdgcn_mfma_f32_32x32x16_bf16(pa3, PK(c3, d3), o1, 0, 0, 0);
;     ...
; }
; template <bool FIRST> DEVI bool partialSM(f32x16& p0, f32x16& p1, float& m_reg, float& alpha) {
;     float pmax = p0[0];
; #pragma unroll
;     for (int r = 1; r < 16; ++r) pmax = fmaxf(pmax, p0[r]);
; #pragma unroll
;     for (int r = 0; r < 16; ++r) pmax = fmaxf(pmax, p1[r]);
;     { auto rr = __builtin_amdgcn_permlane32_swap(__float_as_uint(pmax), __float_as_uint(pmax), false, false);
;       pmax = fmaxf(__uint_as_float(rr[0]), __uint_as_float(rr[1])); }
;     if (FIRST) { m_reg = pmax; alpha = 1.f;
; #pragma unroll
;         for (int r = 0; r < 16; ++r) { p0[r] = __builtin_amdgcn_exp2f(p0[r] - pmax); p1[r] = p1[r] - pmax; }
;         return false;
;     } else if (__builtin_expect(__all(pmax <= ATT_THR), 1)) { alpha = 1.f;
; #pragma unroll
;         for (int r = 0; r < 16; ++r) p0[r] = __builtin_amdgcn_exp2f(p0[r]);
	v_mfma_f32_32x32x16_bf16 v[98:113], v[234:237], v[146:149], v[98:113]
	v_add_f32_e64 v126, v212, v126
	v_add_f32_e64 v127, v213, v127
	v_add_f32_e64 v212, v60, v76
	v_add_f32_e64 v213, v61, v77
	v_cvt_pk_bf16_f32 v60, v70, v71
	v_cvt_pk_bf16_f32 v61, v72, v73
	v_add_f32_e64 v126, v212, v126
	v_add_f32_e64 v127, v213, v127
	v_add_f32_e32 v212, v62, v78
	v_add_f32_e32 v213, v63, v79
	v_cvt_pk_bf16_f32 v62, v74, v75
	v_cvt_pk_bf16_f32 v63, v76, v77
	v_mfma_f32_32x32x16_bf16 v[82:97], v[224:227], v[146:149], v[82:97]
	v_add_f32_e64 v126, v212, v126
	v_add_f32_e64 v127, v213, v127
	v_add_f32_e64 v212, v64, v80
	v_add_f32_e64 v213, v65, v81
	v_cvt_pk_bf16_f32 v64, v78, v79
	v_cvt_pk_bf16_f32 v65, v80, v81
	ds_read_b64_tr_b16 v[66:67], v174 offset:0
	ds_read_b64_tr_b16 v[68:69], v174 offset:0x400
	ds_read_b64_tr_b16 v[70:71], v174 offset:0x800
	ds_read_b64_tr_b16 v[72:73], v174 offset:0xc00
	ds_read_b64_tr_b16 v[74:75], v174 offset:0x1000
	ds_read_b64_tr_b16 v[76:77], v174 offset:0x1400
	ds_read_b64_tr_b16 v[78:79], v174 offset:0x1800
	ds_read_b64_tr_b16 v[80:81], v174 offset:0x1c00
	v_add_f32_e64 v126, v212, v126
	v_add_f32_e64 v127, v213, v127
	ds_read_b64_tr_b16 v[212:213], v174 offset:0x200
	ds_read_b64_tr_b16 v[214:215], v174 offset:0x600
	ds_read_b64_tr_b16 v[216:217], v174 offset:0xa00
	v_mfma_f32_32x32x16_bf16 v[98:113], v[228:231], v[142:145], v[98:113]
	ds_read_b64_tr_b16 v[218:219], v174 offset:0xe00
	ds_read_b64_tr_b16 v[220:221], v174 offset:0x1200
	ds_read_b64_tr_b16 v[222:223], v174 offset:0x1600
	ds_read_b64_tr_b16 v[224:225], v174 offset:0x1a00
	ds_read_b64_tr_b16 v[226:227], v174 offset:0x1e00
	v_add_f32_e32 v126, v126, v127
	v_mfma_f32_32x32x16_bf16 v[82:97], v[232:235], v[142:145], v[82:97]
	v_mov_b32_e32 v127, v126
	s_nop 1
	v_permlane32_swap_b32_e32 v126, v127
	s_waitcnt lgkmcnt(14)
	v_mfma_f32_32x32x16_bf16 v[18:33], v[50:53], v[66:69], v[18:33]
	s_waitcnt lgkmcnt(6)
	v_mfma_f32_32x32x16_bf16 v[2:17], v[50:53], v[212:215], v[2:17]
	s_nop 4
	v_max_f32_e32 v249, v99, v99
	v_max_f32_e32 v250, v98, v98
	v_max_f32_e32 v249, v250, v249
	v_max3_f32 v249, v249, v100, v101
	v_max3_f32 v249, v249, v102, v103
	v_max3_f32 v251, v249, v104, v105
	v_max3_f32 v251, v251, v106, v107
	v_exp_f32_e32 v50, v98
	v_exp_f32_e32 v51, v99
	v_exp_f32_e32 v52, v100
	v_exp_f32_e32 v53, v101
	v_mov_b64_e32 v[66:67], v[82:83]
	v_mov_b64_e32 v[68:69], v[84:85]
	v_mfma_f32_32x32x16_bf16 v[18:33], v[54:57], v[70:73], v[18:33]
	s_waitcnt lgkmcnt(4)
	v_mfma_f32_32x32x16_bf16 v[2:17], v[54:57], v[216:219], v[2:17]
	v_max3_f32 v251, v251, v108, v109
	v_max3_f32 v251, v251, v110, v111
	v_max3_f32 v251, v251, v112, v113
	v_max3_f32 v251, v251, v82, v83
	v_max3_f32 v251, v251, v84, v85
	v_max3_f32 v251, v251, v86, v87
	v_max3_f32 v251, v251, v88, v89
	v_exp_f32_e32 v54, v102
	v_exp_f32_e32 v55, v103
	v_exp_f32_e32 v56, v104
	v_exp_f32_e32 v57, v105
	v_mov_b64_e32 v[70:71], v[86:87]
	v_mov_b64_e32 v[72:73], v[88:89]
	v_mfma_f32_32x32x16_bf16 v[18:33], v[58:61], v[74:77], v[18:33]
	s_waitcnt lgkmcnt(2)
	v_mfma_f32_32x32x16_bf16 v[2:17], v[58:61], v[220:223], v[2:17]
	v_max3_f32 v251, v251, v90, v91
	v_max3_f32 v251, v251, v92, v93
	v_max3_f32 v251, v251, v94, v95
	v_max3_f32 v251, v251, v96, v97
	v_mov_b32_e32 v252, v251
	s_nop 1
	v_permlane32_swap_b32_e32 v251, v252
	v_exp_f32_e32 v58, v106
	v_exp_f32_e32 v59, v107
	v_exp_f32_e32 v60, v108
	v_exp_f32_e32 v61, v109
	v_mov_b64_e32 v[74:75], v[90:91]
	v_mov_b64_e32 v[76:77], v[92:93]
	v_mfma_f32_32x32x16_bf16 v[18:33], v[62:65], v[78:81], v[18:33]
	s_waitcnt lgkmcnt(0)
	v_mfma_f32_32x32x16_bf16 v[2:17], v[62:65], v[224:227], v[2:17]
	v_exp_f32_e32 v62, v110
	v_exp_f32_e32 v63, v111
	v_exp_f32_e32 v64, v112
	v_exp_f32_e32 v65, v113
	v_mov_b64_e32 v[78:79], v[94:95]
	v_mov_b64_e32 v[80:81], v[96:97]
	v_max_f32_e32 v252, v252, v252
	v_max_f32_e32 v251, v251, v251
	v_max_f32_e32 v174, v251, v252
	v_cmp_ge_f32_e32 vcc, s80, v174
	s_cmp_lg_u64 vcc, exec
	s_cselect_b64 s[6:7], -1, 0
	s_cbranch_scc1 .LBB0_2275
	v_mov_b32_e32 v203, 1.0
	v_mov_b32_e32 v204, v210
	s_branch .LBB0_2280
